# grid barrier: L1 invalidate issued by wave 1 at arrival instead of by the leader after release
# speedup vs baseline: 1.0132x; 1.0132x over previous
.LBB0_190:
	s_or_b64 exec, exec, s[4:5]
	v_readlane_b32 s4, v254, 16
	v_readlane_b32 s5, v254, 17
	s_waitcnt vmcnt(0)
	s_nop 2
	global_atomic_add v209, v231, s[4:5]
	s_waitcnt vmcnt(0)

.LBB0_204:
	s_waitcnt vmcnt(0)
	s_waitcnt vmcnt(0)
	s_barrier
	v_readlane_b32 s2, v254, 9
	s_nop 0
	s_cmp_lg_u32 s2, 64
	s_cbranch_scc1 .Lbinv_0
	buffer_inv sc1
	s_waitcnt vmcnt(0)
.Lbinv_0:
	s_and_saveexec_b64 s[2:3], s[4:5]
	s_cbranch_execz .LBB0_251
	v_readlane_b32 s4, v254, 22
	s_waitcnt vmcnt(0) expcnt(0) lgkmcnt(0)
	s_nop 0
	v_mov_b32_e32 v0, s4
	ds_read_b32 v2, v0
	v_readlane_b32 s4, v254, 23
	s_waitcnt lgkmcnt(0)
	v_cmp_ne_u32_e32 vcc, 0, v2
	v_mov_b32_e32 v0, s4
	ds_read_b32 v0, v0
	s_cbranch_vccnz .LBB0_219
	v_readlane_b32 s6, v254, 0
	v_readlane_b32 s7, v254, 1
	s_load_dwordx2 s[4:5], s[6:7], 0x4
	s_mov_b32 s10, 0
	s_waitcnt lgkmcnt(0)
	s_mul_i32 s9, s4, s91
	s_mul_i32 s9, s9, s5
	s_branch .LBB0_208

.LBB0_232:
	s_or_b64 exec, exec, s[6:7]
	s_waitcnt vmcnt(0)
	s_waitcnt vmcnt(0)

.LBB0_280:
	s_waitcnt vmcnt(0)
	s_waitcnt vmcnt(0) lgkmcnt(0)
	s_barrier
	v_readlane_b32 s4, v254, 9
	s_nop 0
	s_cmp_lg_u32 s4, 64
	s_cbranch_scc1 .Lbinv_1
	buffer_inv sc1
	s_waitcnt vmcnt(0)
.Lbinv_1:
	s_and_saveexec_b64 s[4:5], s[6:7]
	s_cbranch_execz .LBB0_328
	v_readlane_b32 s3, v254, 22
	s_waitcnt vmcnt(0) expcnt(0) lgkmcnt(0)
	s_nop 0
	v_mov_b32_e32 v0, s3
	ds_read_b32 v2, v0
	v_readlane_b32 s3, v254, 23
	s_waitcnt lgkmcnt(0)
	v_cmp_ne_u32_e32 vcc, 0, v2
	v_mov_b32_e32 v0, s3
	ds_read_b32 v0, v0
	s_cbranch_vccnz .LBB0_296
	v_readlane_b32 s8, v254, 0
	v_readlane_b32 s9, v254, 1
	s_load_dwordx2 s[6:7], s[8:9], 0x4
	s_mov_b32 s11, 0
	s_waitcnt lgkmcnt(0)
	s_mul_i32 s10, s6, s91
	s_mul_i32 s10, s10, s7
	s_branch .LBB0_284

.LBB0_309:
	s_or_b64 exec, exec, s[8:9]
	s_waitcnt vmcnt(0)
	s_waitcnt vmcnt(0)

.LBB0_327:
	s_or_b64 exec, exec, s[6:7]
	v_readlane_b32 s6, v254, 16
	v_readlane_b32 s7, v254, 17
	s_waitcnt vmcnt(0)
	s_nop 2
	global_atomic_add v209, v231, s[6:7]
	s_waitcnt vmcnt(0)

.Lbinv_3:
	s_and_saveexec_b64 s[4:5], s[8:9]
	s_cbranch_execz .LBB0_517
	v_readlane_b32 s2, v254, 22
	s_waitcnt vmcnt(0) expcnt(0) lgkmcnt(0)
	s_nop 0
	v_mov_b32_e32 v0, s2
	ds_read_b32 v2, v0
	v_readlane_b32 s2, v254, 23
	s_waitcnt lgkmcnt(0)
	v_cmp_ne_u32_e32 vcc, 0, v2
	v_mov_b32_e32 v0, s2
	ds_read_b32 v0, v0
	s_cbranch_vccnz .LBB0_485
	v_readlane_b32 s8, v254, 0
	v_readlane_b32 s9, v254, 1
	s_load_dwordx2 s[2:3], s[8:9], 0x4
	s_mov_b32 s12, 0
	s_waitcnt lgkmcnt(0)
	s_mul_i32 s2, s2, s91
	s_mul_i32 s3, s2, s3
	s_branch .LBB0_474

.LBB0_498:
	s_or_b64 exec, exec, s[10:11]
	s_waitcnt vmcnt(0)
	s_waitcnt vmcnt(0)

.LBB0_516:
	s_or_b64 exec, exec, s[8:9]
	v_readlane_b32 s2, v254, 16
	v_readlane_b32 s3, v254, 17
	s_waitcnt vmcnt(0)
	s_nop 2
	global_atomic_add v209, v231, s[2:3]
	s_waitcnt vmcnt(0)

.LBB0_537:
	s_waitcnt vmcnt(0)
	s_waitcnt vmcnt(0) lgkmcnt(0)
	s_barrier
	v_readlane_b32 s2, v254, 9
	s_nop 0
	s_cmp_lg_u32 s2, 64
	s_cbranch_scc1 .Lbinv_4
	buffer_inv sc1
	s_waitcnt vmcnt(0)

.Lbinv_9:
	s_and_saveexec_b64 s[2:3], s[4:5]
	v_readlane_b32 s62, v254, 6
	v_readlane_b32 s63, v254, 7
	v_readlane_b32 s91, v254, 8
	s_cbranch_execz .LBB0_1069
	v_readlane_b32 s4, v254, 22
	s_waitcnt vmcnt(0) expcnt(0) lgkmcnt(0)
	s_nop 0
	v_mov_b32_e32 v0, s4
	ds_read_b32 v2, v0
	v_readlane_b32 s4, v254, 23
	s_waitcnt lgkmcnt(0)
	v_cmp_ne_u32_e32 vcc, 0, v2
	v_mov_b32_e32 v0, s4
	ds_read_b32 v0, v0
	s_cbranch_vccnz .LBB0_1022
	v_readlane_b32 s6, v254, 0
	v_readlane_b32 s7, v254, 1
	s_load_dwordx2 s[4:5], s[6:7], 0x4
	s_mov_b32 s10, 0
	s_waitcnt lgkmcnt(0)
	s_mul_i32 s9, s4, s91
	s_mul_i32 s9, s9, s5
	s_branch .LBB0_1010

.LBB0_1296:
	s_waitcnt vmcnt(0)
	s_barrier
	v_readlane_b32 s2, v254, 9
	s_nop 0
	s_cmp_lg_u32 s2, 64
	s_cbranch_scc1 .Lbinv_10
	buffer_inv sc1
	s_waitcnt vmcnt(0)

.Lbinv_12:
	s_and_saveexec_b64 s[2:3], s[4:5]
	s_cbranch_execnz .LBB0_1454
	s_getpc_b64 s[98:99]
